# prologue memory-token norm: the 16 gain loads hoisted ahead of the row math, counted waits (vmcnt 15) instead of a full drain per step
# speedup vs baseline: 1.0399x; 1.0079x over previous
; __device__ __forceinline__ unsigned cvt_pk_bf16(float lo, float hi) { unsigned r; asm volatile("v_cvt_pk_bf16_f32 %0, %1, %2" : "=v"(r) : "v"(lo), "v"(hi)); return r; }
; __device__ __forceinline__ void rms_row_bf16(const float4 (&v)[4], float rs, const float* g, bf16* dst, int lane) {
; #pragma unroll
;     for (int j = 0; j < 4; ++j) { const float4 gg = g ? ((const float4*)g)[lane + 64 * j] : make_float4(1.f, 1.f, 1.f, 1.f);
;         u32x2 w; w.x = cvt_pk_bf16(v[j].x * rs * gg.x, v[j].y * rs * gg.y); w.y = cvt_pk_bf16(v[j].z * rs * gg.z, v[j].w * rs * gg.w); ((u32x2*)dst)[lane + 64 * j] = w; }
; template <int PH, bool PRB = false>
; __device__ __forceinline__ void run_phase(int layer, LAS unsigned char* lds, const int wv_) {
;     ...
;         for (int r = gw; r < MEM; r += NGW) {
;             const float4* s4 = (const float4*)(p.mem + (size_t)r * D); float4 v[4]; float ss = 0.f;
; #pragma unroll
;             for (int j = 0; j < 4; ++j) { v[j] = s4[lane + 64 * j]; ss += v[j].x * v[j].x + v[j].y * v[j].y + v[j].z * v[j].z + v[j].w * v[j].w; }
;             const float rs = rsqrtf(wave_sum(ss) * (1.0f / D) + 1e-6f);
;             for (int l = 0; l < DEPTH; ++l) rms_row_bf16(v, rs, p.ln_mem + l * D, memn + ((size_t)l * MEM + r) * D, lane);
.LBB0_47:
	s_waitcnt vmcnt(15)
	v_mul_f32_e32 v2, v15, v2
	v_mul_f32_e32 v3, v14, v3
	v_cvt_pk_bf16_f32 v2, v2, v3
	v_mul_f32_e32 v3, v12, v4
	s_add_i32 s9, s9, s90
	v_mul_f32_e32 v4, v13, v5
	v_cvt_pk_bf16_f32 v3, v3, v4
	global_store_dwordx2 v[52:53], v[2:3], off
	v_lshl_add_u64 v[52:53], v[52:53], 0, s[0:1]
	s_cmpk_gt_i32 s9, 0xff
	v_lshl_add_u64 v[54:55], v[54:55], 0, s[6:7]
	s_cbranch_scc1 .LBB0_80
.LBB0_48:
	global_load_dwordx4 v[14:17], v[54:55], off nt
	global_load_dwordx4 v[10:13], v[54:55], off offset:1024 nt
	global_load_dwordx4 v[6:9], v[54:55], off offset:2048 nt
	global_load_dwordx4 v[2:5], v[54:55], off offset:3072 nt
	s_and_b64 vcc, exec, s[4:5]
	s_cbranch_vccnz .Lmemn_nopf
	global_load_dwordx4 v[128:131], v[24:25], off
	global_load_dwordx4 v[132:135], v[24:25], off offset:1024
	global_load_dwordx4 v[136:139], v[24:25], off offset:2048
	global_load_dwordx4 v[140:143], v[24:25], off offset:3072
	global_load_dwordx4 v[144:147], v[26:27], off
	global_load_dwordx4 v[148:151], v[28:29], off
	global_load_dwordx4 v[152:155], v[30:31], off
	global_load_dwordx4 v[156:159], v[32:33], off
	global_load_dwordx4 v[160:163], v[36:37], off
	global_load_dwordx4 v[164:167], v[38:39], off
	global_load_dwordx4 v[168:171], v[40:41], off
	global_load_dwordx4 v[172:175], v[42:43], off
	global_load_dwordx4 v[176:179], v[44:45], off
	global_load_dwordx4 v[180:183], v[46:47], off
	global_load_dwordx4 v[184:187], v[48:49], off
	global_load_dwordx4 v[188:191], v[50:51], off
	s_branch .Lmemn_pfdone

; __device__ __forceinline__ unsigned cvt_pk_bf16(float lo, float hi) { unsigned r; asm volatile("v_cvt_pk_bf16_f32 %0, %1, %2" : "=v"(r) : "v"(lo), "v"(hi)); return r; }
; __device__ __forceinline__ void rms_row_bf16(const float4 (&v)[4], float rs, const float* g, bf16* dst, int lane) {
; #pragma unroll
;     for (int j = 0; j < 4; ++j) { const float4 gg = g ? ((const float4*)g)[lane + 64 * j] : make_float4(1.f, 1.f, 1.f, 1.f);
;         u32x2 w; w.x = cvt_pk_bf16(v[j].x * rs * gg.x, v[j].y * rs * gg.y); w.y = cvt_pk_bf16(v[j].z * rs * gg.z, v[j].w * rs * gg.w); ((u32x2*)dst)[lane + 64 * j] = w; }
; template <int PH, bool PRB = false>
; __device__ __forceinline__ void run_phase(int layer, LAS unsigned char* lds, const int wv_) {
;     ...
;         for (int r = gw; r < MEM; r += NGW) {
;             const float4* s4 = (const float4*)(p.mem + (size_t)r * D); float4 v[4]; float ss = 0.f;
; #pragma unroll
;             for (int j = 0; j < 4; ++j) { v[j] = s4[lane + 64 * j]; ss += v[j].x * v[j].x + v[j].y * v[j].y + v[j].z * v[j].z + v[j].w * v[j].w; }
;             const float rs = rsqrtf(wave_sum(ss) * (1.0f / D) + 1e-6f);
;             for (int l = 0; l < DEPTH; ++l) rms_row_bf16(v, rs, p.ln_mem + l * D, memn + ((size_t)l * MEM + r) * D, lane);
.Lmemn_pfdone:
	s_and_b64 vcc, exec, s[4:5]
	v_mov_b32_e32 v22, 1.0
	v_mov_b32_e32 v23, 1.0
	s_waitcnt vmcnt(19)
	v_mul_f32_e32 v18, v15, v15
	s_waitcnt vmcnt(18)
	v_mul_f32_e32 v19, v11, v11
	s_waitcnt vmcnt(17)
	v_mul_f32_e32 v20, v7, v7
	v_fmac_f32_e32 v18, v14, v14
	v_fmac_f32_e32 v19, v10, v10
	s_waitcnt vmcnt(16)
	v_mul_f32_e32 v21, v3, v3
	v_fmac_f32_e32 v20, v6, v6
	v_fmac_f32_e32 v18, v16, v16
	v_fmac_f32_e32 v19, v12, v12
	v_fmac_f32_e32 v21, v2, v2
	v_fmac_f32_e32 v20, v8, v8
	v_fmac_f32_e32 v18, v17, v17
	v_fmac_f32_e32 v19, v13, v13
	v_fmac_f32_e32 v21, v4, v4
	v_fmac_f32_e32 v20, v9, v9
	v_add_f32_e32 v18, v18, v19
	v_fmac_f32_e32 v21, v5, v5
	v_add_f32_e32 v18, v18, v20
	v_add_f32_e32 v18, v18, v21
	ds_swizzle_b32 v19, v18 offset:swizzle(SWAP,1)
	s_waitcnt lgkmcnt(0)
	v_add_f32_e32 v18, v18, v19
	ds_swizzle_b32 v19, v18 offset:swizzle(SWAP,2)
	s_waitcnt lgkmcnt(0)
	v_add_f32_e32 v18, v18, v19
	ds_swizzle_b32 v19, v18 offset:swizzle(SWAP,4)
	s_waitcnt lgkmcnt(0)
	v_add_f32_e32 v19, v18, v19
	ds_swizzle_b32 v20, v19 offset:swizzle(SWAP,8)
	v_mov_b32_e32 v18, 1.0
	s_waitcnt lgkmcnt(0)
	v_add_f32_e32 v19, v19, v20
	ds_swizzle_b32 v21, v19 offset:swizzle(SWAP,16)
	v_mov_b32_e32 v20, 1.0
	s_waitcnt lgkmcnt(0)
	v_add_f32_e32 v19, v19, v21
	v_mov_b32_e32 v57, v19
	s_nop 1
	v_permlane32_swap_b32_e32 v19, v57
	v_mov_b32_e32 v21, 1.0
	s_cbranch_vccnz .LBB0_50
	s_waitcnt vmcnt(15)
	v_mov_b64_e32 v[20:21], v[128:129]
	v_mov_b64_e32 v[22:23], v[130:131]
.LBB0_50:
	v_add_f32_e32 v19, v19, v57
	v_fmamk_f32 v19, v19, 0x3a800000, v35
	v_mul_f32_e32 v57, 0x4b800000, v19
	v_cmp_gt_f32_e32 vcc, s8, v19
	s_nop 1
	v_cndmask_b32_e32 v19, v19, v57, vcc
	v_rsq_f32_e32 v19, v19
	s_nop 0
	v_mul_f32_e32 v57, 0x45800000, v19
	v_cndmask_b32_e32 v61, v19, v57, vcc
	v_mul_f32_e32 v60, v14, v61
	v_mul_f32_e32 v59, v15, v61
	v_mul_f32_e32 v57, v16, v61
	v_mul_f32_e32 v58, v17, v61
	s_waitcnt vmcnt(15)
	v_mul_f32_e32 v14, v60, v20
	v_mul_f32_e32 v15, v59, v21
	v_cvt_pk_bf16_f32 v14, v14, v15
	v_mul_f32_e32 v15, v57, v22
	v_mul_f32_e32 v16, v58, v23
	v_cvt_pk_bf16_f32 v15, v15, v16
	v_add_co_u32_e32 v16, vcc, 0xffe80000, v52
	v_mov_b32_e32 v19, 1.0
	s_nop 0
	v_addc_co_u32_e32 v17, vcc, -1, v53, vcc
	global_store_dwordx2 v[16:17], v[14:15], off offset:-1536
	s_and_b64 vcc, exec, s[4:5]
	v_mov_b32_e32 v16, 1.0
	v_mov_b32_e32 v17, 1.0
	s_cbranch_vccnz .LBB0_52
	s_waitcnt vmcnt(15)
	v_mov_b64_e32 v[16:17], v[132:133]
	v_mov_b64_e32 v[18:19], v[134:135]
.LBB0_52:
	v_mul_f32_e32 v23, v10, v61
	v_mul_f32_e32 v22, v11, v61
	v_mul_f32_e32 v20, v12, v61
	v_mul_f32_e32 v21, v13, v61
	s_waitcnt vmcnt(15)
	v_mul_f32_e32 v10, v23, v16
	v_mul_f32_e32 v11, v22, v17
	v_cvt_pk_bf16_f32 v10, v10, v11
	v_mul_f32_e32 v11, v20, v18
	v_mul_f32_e32 v12, v21, v19
	v_cvt_pk_bf16_f32 v11, v11, v12
	v_add_co_u32_e32 v12, vcc, 0xffe80000, v52
	v_mov_b32_e32 v14, 1.0
	s_nop 0
	v_addc_co_u32_e32 v13, vcc, -1, v53, vcc
	global_store_dwordx2 v[12:13], v[10:11], off offset:-1024
	v_mov_b32_e32 v10, 1.0
	s_and_b64 vcc, exec, s[4:5]
	v_mov_b32_e32 v15, 1.0
	v_mov_b32_e32 v12, 1.0
	v_mov_b32_e32 v13, 1.0
	s_cbranch_vccnz .LBB0_54
	s_waitcnt vmcnt(15)
	v_mov_b64_e32 v[12:13], v[136:137]
	v_mov_b64_e32 v[14:15], v[138:139]
.LBB0_54:
	v_mul_f32_e32 v19, v6, v61
	v_mul_f32_e32 v18, v7, v61
	v_mul_f32_e32 v16, v8, v61
	v_mul_f32_e32 v17, v9, v61
	s_waitcnt vmcnt(15)
	v_mul_f32_e32 v6, v19, v12
	v_mul_f32_e32 v7, v18, v13
	v_cvt_pk_bf16_f32 v6, v6, v7
	v_mul_f32_e32 v7, v16, v14
	v_mul_f32_e32 v8, v17, v15
	v_cvt_pk_bf16_f32 v7, v7, v8
	v_add_co_u32_e32 v8, vcc, 0xffe80000, v52
	v_mov_b32_e32 v11, 1.0
	s_nop 0
	v_addc_co_u32_e32 v9, vcc, -1, v53, vcc
	global_store_dwordx2 v[8:9], v[6:7], off offset:-512
	s_and_b64 vcc, exec, s[4:5]
	v_mov_b32_e32 v8, 1.0
	v_mov_b32_e32 v9, 1.0
	s_cbranch_vccnz .LBB0_56
	s_waitcnt vmcnt(15)
	v_mov_b64_e32 v[8:9], v[140:141]
	v_mov_b64_e32 v[10:11], v[142:143]
.LBB0_56:
	v_mul_f32_e32 v15, v2, v61
	v_mul_f32_e32 v14, v3, v61
	v_mul_f32_e32 v12, v4, v61
	v_mul_f32_e32 v13, v5, v61
	s_waitcnt vmcnt(15)
	v_mul_f32_e32 v2, v15, v8
	v_mul_f32_e32 v3, v14, v9
	v_cvt_pk_bf16_f32 v2, v2, v3
	v_mul_f32_e32 v3, v12, v10
	v_mul_f32_e32 v4, v13, v11
	v_cvt_pk_bf16_f32 v3, v3, v4
	v_add_co_u32_e32 v4, vcc, 0xffe80000, v52
	v_mov_b32_e32 v8, 1.0
	s_nop 0
	v_addc_co_u32_e32 v5, vcc, -1, v53, vcc
	global_store_dwordx2 v[4:5], v[2:3], off
	v_mov_b32_e32 v4, 1.0
	s_and_b64 vcc, exec, s[4:5]
	v_mov_b32_e32 v9, 1.0
	v_mov_b32_e32 v6, 1.0
	v_mov_b32_e32 v7, 1.0
	s_cbranch_vccnz .LBB0_58
	s_waitcnt vmcnt(15)
	v_mov_b64_e32 v[6:7], v[144:145]
	v_mov_b64_e32 v[8:9], v[146:147]
.LBB0_58:
	s_waitcnt vmcnt(15)
	v_mul_f32_e32 v2, v60, v6
	v_mul_f32_e32 v3, v59, v7
	v_cvt_pk_bf16_f32 v2, v2, v3
	v_mul_f32_e32 v3, v57, v8
	v_add_co_u32_e32 v6, vcc, 0xfff00000, v52
	v_mul_f32_e32 v5, v58, v9
	v_cvt_pk_bf16_f32 v3, v3, v5
	s_nop 0
	v_addc_co_u32_e32 v7, vcc, -1, v53, vcc
	global_store_dwordx2 v[6:7], v[2:3], off offset:-1536
	s_and_b64 vcc, exec, s[4:5]
	v_mov_b32_e32 v5, 1.0
	v_mov_b32_e32 v2, 1.0
	v_mov_b32_e32 v3, 1.0
	s_cbranch_vccnz .LBB0_60
	s_waitcnt vmcnt(15)
	v_mov_b64_e32 v[2:3], v[148:149]
	v_mov_b64_e32 v[4:5], v[150:151]
; __device__ __forceinline__ unsigned cvt_pk_bf16(float lo, float hi) { unsigned r; asm volatile("v_cvt_pk_bf16_f32 %0, %1, %2" : "=v"(r) : "v"(lo), "v"(hi)); return r; }
; __device__ __forceinline__ void rms_row_bf16(const float4 (&v)[4], float rs, const float* g, bf16* dst, int lane) {
; #pragma unroll
;     for (int j = 0; j < 4; ++j) { const float4 gg = g ? ((const float4*)g)[lane + 64 * j] : make_float4(1.f, 1.f, 1.f, 1.f);
;         u32x2 w; w.x = cvt_pk_bf16(v[j].x * rs * gg.x, v[j].y * rs * gg.y); w.y = cvt_pk_bf16(v[j].z * rs * gg.z, v[j].w * rs * gg.w); ((u32x2*)dst)[lane + 64 * j] = w; }
; template <int PH, bool PRB = false>
; __device__ __forceinline__ void run_phase(int layer, LAS unsigned char* lds, const int wv_) {
;     ...
;             const float rs = rsqrtf(wave_sum(ss) * (1.0f / D) + 1e-6f);
;             for (int l = 0; l < DEPTH; ++l) rms_row_bf16(v, rs, p.ln_mem + l * D, memn + ((size_t)l * MEM + r) * D, lane);
.LBB0_60:
	s_waitcnt vmcnt(15)
	v_mul_f32_e32 v2, v23, v2
	v_mul_f32_e32 v3, v22, v3
	v_cvt_pk_bf16_f32 v2, v2, v3
	v_mul_f32_e32 v3, v20, v4
	v_mul_f32_e32 v4, v21, v5
	v_cvt_pk_bf16_f32 v3, v3, v4
	v_add_co_u32_e32 v4, vcc, 0xfff00000, v52
	v_mov_b32_e32 v8, 1.0
	s_nop 0
	v_addc_co_u32_e32 v5, vcc, -1, v53, vcc
	global_store_dwordx2 v[4:5], v[2:3], off offset:-1024
	v_mov_b32_e32 v4, 1.0
	s_and_b64 vcc, exec, s[4:5]
	v_mov_b32_e32 v9, 1.0
	v_mov_b32_e32 v6, 1.0
	v_mov_b32_e32 v7, 1.0
	s_cbranch_vccnz .LBB0_62
	s_waitcnt vmcnt(15)
	v_mov_b64_e32 v[6:7], v[152:153]
	v_mov_b64_e32 v[8:9], v[154:155]
.LBB0_62:
	s_waitcnt vmcnt(15)
	v_mul_f32_e32 v2, v19, v6
	v_mul_f32_e32 v3, v18, v7
	v_cvt_pk_bf16_f32 v2, v2, v3
	v_mul_f32_e32 v3, v16, v8
	v_add_co_u32_e32 v6, vcc, 0xfff00000, v52
	v_mul_f32_e32 v5, v17, v9
	v_cvt_pk_bf16_f32 v3, v3, v5
	s_nop 0
	v_addc_co_u32_e32 v7, vcc, -1, v53, vcc
	global_store_dwordx2 v[6:7], v[2:3], off offset:-512
	s_and_b64 vcc, exec, s[4:5]
	v_mov_b32_e32 v5, 1.0
	v_mov_b32_e32 v2, 1.0
	v_mov_b32_e32 v3, 1.0
	s_cbranch_vccnz .LBB0_64
	s_waitcnt vmcnt(15)
	v_mov_b64_e32 v[2:3], v[156:157]
	v_mov_b64_e32 v[4:5], v[158:159]
.LBB0_64:
	s_waitcnt vmcnt(15)
	v_mul_f32_e32 v2, v15, v2
	v_mul_f32_e32 v3, v14, v3
	v_cvt_pk_bf16_f32 v2, v2, v3
	v_mul_f32_e32 v3, v12, v4
	v_mul_f32_e32 v4, v13, v5
	v_cvt_pk_bf16_f32 v3, v3, v4
	v_add_co_u32_e32 v4, vcc, 0xfff00000, v52
	v_mov_b32_e32 v8, 1.0
	s_nop 0
	v_addc_co_u32_e32 v5, vcc, -1, v53, vcc
	global_store_dwordx2 v[4:5], v[2:3], off
	v_mov_b32_e32 v4, 1.0
	s_and_b64 vcc, exec, s[4:5]
	v_mov_b32_e32 v9, 1.0
	v_mov_b32_e32 v6, 1.0
	v_mov_b32_e32 v7, 1.0
	s_cbranch_vccnz .LBB0_66
	s_waitcnt vmcnt(15)
	v_mov_b64_e32 v[6:7], v[160:161]
	v_mov_b64_e32 v[8:9], v[162:163]
.LBB0_66:
	s_waitcnt vmcnt(15)
	v_mul_f32_e32 v2, v60, v6
	v_mul_f32_e32 v3, v59, v7
	v_cvt_pk_bf16_f32 v2, v2, v3
	v_mul_f32_e32 v3, v57, v8
	v_add_co_u32_e32 v6, vcc, 0xfff80000, v52
	v_mul_f32_e32 v5, v58, v9
	v_cvt_pk_bf16_f32 v3, v3, v5
	s_nop 0
	v_addc_co_u32_e32 v7, vcc, -1, v53, vcc
	global_store_dwordx2 v[6:7], v[2:3], off offset:-1536
	s_and_b64 vcc, exec, s[4:5]
	v_mov_b32_e32 v5, 1.0
	v_mov_b32_e32 v2, 1.0
	v_mov_b32_e32 v3, 1.0
	s_cbranch_vccnz .LBB0_68
	s_waitcnt vmcnt(15)
	v_mov_b64_e32 v[2:3], v[164:165]
	v_mov_b64_e32 v[4:5], v[166:167]
.LBB0_68:
	s_waitcnt vmcnt(15)
	v_mul_f32_e32 v2, v23, v2
	v_mul_f32_e32 v3, v22, v3
	v_cvt_pk_bf16_f32 v2, v2, v3
	v_mul_f32_e32 v3, v20, v4
	v_mul_f32_e32 v4, v21, v5
	v_cvt_pk_bf16_f32 v3, v3, v4
	v_add_co_u32_e32 v4, vcc, 0xfff80000, v52
	v_mov_b32_e32 v8, 1.0
	s_nop 0
	v_addc_co_u32_e32 v5, vcc, -1, v53, vcc
	global_store_dwordx2 v[4:5], v[2:3], off offset:-1024
	v_mov_b32_e32 v4, 1.0
	s_and_b64 vcc, exec, s[4:5]
	v_mov_b32_e32 v9, 1.0
	v_mov_b32_e32 v6, 1.0
	v_mov_b32_e32 v7, 1.0
	s_cbranch_vccnz .LBB0_70
	s_waitcnt vmcnt(15)
	v_mov_b64_e32 v[6:7], v[168:169]
	v_mov_b64_e32 v[8:9], v[170:171]
.LBB0_70:
	s_waitcnt vmcnt(15)
	v_mul_f32_e32 v2, v19, v6
	v_mul_f32_e32 v3, v18, v7
	v_cvt_pk_bf16_f32 v2, v2, v3
	v_mul_f32_e32 v3, v16, v8
	v_add_co_u32_e32 v6, vcc, 0xfff80000, v52
	v_mul_f32_e32 v5, v17, v9
	v_cvt_pk_bf16_f32 v3, v3, v5
	s_nop 0
	v_addc_co_u32_e32 v7, vcc, -1, v53, vcc
	global_store_dwordx2 v[6:7], v[2:3], off offset:-512
	s_and_b64 vcc, exec, s[4:5]
	v_mov_b32_e32 v5, 1.0
	v_mov_b32_e32 v2, 1.0
	v_mov_b32_e32 v3, 1.0
	s_cbranch_vccnz .LBB0_72
	s_waitcnt vmcnt(15)
	v_mov_b64_e32 v[2:3], v[172:173]
	v_mov_b64_e32 v[4:5], v[174:175]
.LBB0_72:
	s_waitcnt vmcnt(15)
	v_mul_f32_e32 v2, v15, v2
	v_mul_f32_e32 v3, v14, v3
	v_cvt_pk_bf16_f32 v2, v2, v3
	v_mul_f32_e32 v3, v12, v4
	v_mul_f32_e32 v4, v13, v5
	v_cvt_pk_bf16_f32 v3, v3, v4
	v_add_co_u32_e32 v4, vcc, 0xfff80000, v52
	v_mov_b32_e32 v8, 1.0
	s_nop 0
	v_addc_co_u32_e32 v5, vcc, -1, v53, vcc
	global_store_dwordx2 v[4:5], v[2:3], off
	v_mov_b32_e32 v4, 1.0
	s_and_b64 vcc, exec, s[4:5]
	v_mov_b32_e32 v9, 1.0
	v_mov_b32_e32 v6, 1.0
	v_mov_b32_e32 v7, 1.0
	s_cbranch_vccnz .LBB0_74
	s_waitcnt vmcnt(15)
	v_mov_b64_e32 v[6:7], v[176:177]
	v_mov_b64_e32 v[8:9], v[178:179]
.LBB0_74:
	s_waitcnt vmcnt(15)
	v_mul_f32_e32 v2, v60, v6
	v_mul_f32_e32 v3, v59, v7
	v_cvt_pk_bf16_f32 v2, v2, v3
	v_mul_f32_e32 v3, v57, v8
	v_mul_f32_e32 v5, v58, v9
	v_cvt_pk_bf16_f32 v3, v3, v5
	global_store_dwordx2 v[52:53], v[2:3], off offset:-1536
	s_and_b64 vcc, exec, s[4:5]
	v_mov_b32_e32 v5, 1.0
	v_mov_b32_e32 v2, 1.0
	v_mov_b32_e32 v3, 1.0
	s_cbranch_vccnz .LBB0_76
	s_waitcnt vmcnt(15)
	v_mov_b64_e32 v[2:3], v[180:181]
	v_mov_b64_e32 v[4:5], v[182:183]
.LBB0_76:
	s_waitcnt vmcnt(15)
	v_mul_f32_e32 v2, v23, v2
	v_mul_f32_e32 v3, v22, v3
	v_cvt_pk_bf16_f32 v2, v2, v3
	v_mul_f32_e32 v3, v20, v4
	v_mul_f32_e32 v4, v21, v5
	v_cvt_pk_bf16_f32 v3, v3, v4
	v_mov_b32_e32 v4, 1.0
	s_and_b64 vcc, exec, s[4:5]
	v_mov_b32_e32 v8, 1.0
	v_mov_b32_e32 v9, 1.0
	v_mov_b32_e32 v6, 1.0
	v_mov_b32_e32 v7, 1.0
	global_store_dwordx2 v[52:53], v[2:3], off offset:-1024
	s_cbranch_vccnz .LBB0_78
	s_waitcnt vmcnt(15)
	v_mov_b64_e32 v[6:7], v[184:185]
	v_mov_b64_e32 v[8:9], v[186:187]
.LBB0_78:
	s_waitcnt vmcnt(15)
	v_mul_f32_e32 v2, v19, v6
	v_mul_f32_e32 v3, v18, v7
	v_cvt_pk_bf16_f32 v2, v2, v3
	v_mul_f32_e32 v3, v16, v8
	v_mul_f32_e32 v5, v17, v9
	v_cvt_pk_bf16_f32 v3, v3, v5
	global_store_dwordx2 v[52:53], v[2:3], off offset:-512
	s_and_b64 vcc, exec, s[4:5]
	v_mov_b32_e32 v5, 1.0
	v_mov_b32_e32 v2, 1.0
	v_mov_b32_e32 v3, 1.0
	s_cbranch_vccnz .LBB0_47
	s_waitcnt vmcnt(15)
	v_mov_b64_e32 v[2:3], v[188:189]
	v_mov_b64_e32 v[4:5], v[190:191]
	s_branch .LBB0_47
